# plus 4 conversion units per wave inside the router top-k token loop (loads behind the logits prefetch, packed two token iterations later)
# speedup vs baseline: 1.0095x; 1.0095x over previous
; #define LAS __attribute__((address_space(3)))
; __device__ __forceinline__ void convert_experts(Frame& F, int lo, int hi) {
;     const int gw = F.vcu * 8 + F.wave, NGW = F.G * 8;
;     LAS unsigned char* scr = F.lds + F.wave * 16384;
;     unsigned char* W1t = WSP(F, WS_W1T, unsigned char); unsigned char* W2t = WSP(F, WS_W2T, unsigned char);
;     const float* weg = F.a->in[I_WEG]; const float* weu = F.a->in[I_WEU]; const float* wed = F.a->in[I_WED];
;     const float* wsg = F.a->in[I_WSG]; const float* wsu = F.a->in[I_WSU]; const float* wsd = F.a->in[I_WSD];
;     ...
;     constexpr int NPAIRS = CONV_ITEMS / 2;
;     (void)lo; (void)hi;
;     ...
;     if (gw < NPAIRS) {
;         const int ns = 2 * ((NPAIRS - gw + NGW - 1) / NGW);
;         int sq = 0, r = CONV_RIDX(0);
;         TItem tc, tn; CONV_DESC(r, tc); tn = tc;
.Lcv1_vcu:
	s_lshl_b32 s11, s11, 3
	s_add_u32 s89, s11, s9
	s_lshl_b32 s71, s8, 3
	s_mul_i32 s10, s71, 16
	s_add_u32 s89, s89, s10
	s_mov_b32 s69, s89
	s_add_u32 s86, s84, 0x9180000
	s_addc_u32 s87, s85, 0
	s_add_u32 s84, s84, 0x1100000
	s_addc_u32 s85, s85, 0
	s_mov_b32 s90, 0xc2b8aa3b
	s_cmp_ge_u32 s89, 49344
	s_cbranch_scc1 .Lcv1_done
	s_cmp_lt_u32 s69, 49344
	s_cbranch_scc0 .Lcv1_dummyA1
	s_lshr_b32 s10, s69, 6
	s_and_b32 s12, s69, 63
	s_mul_hi_u32 s14, s10, 0xaaaaaaab
	s_lshr_b32 s14, s14, 1
	s_mul_i32 s11, s14, 3
	s_sub_u32 s11, s10, s11
	s_cmp_lt_u32 s14, 256
	s_cselect_b32 s10, s14, 0
	s_cselect_b64 s[44:45], -1, 0
	s_lshl_b32 s10, s10, 20
	s_cmp_eq_u32 s11, 2
	s_cbranch_scc1 .Lcv1_downA1
	s_cmp_eq_u32 s11, 0
	s_cselect_b64 s[4:5], s[72:73], s[74:75]
	s_cselect_b64 s[38:39], s[78:79], s[80:81]
	s_mov_b32 s94, 0xc3317218
	s_cselect_b32 s94, s90, s94
	s_cmp_lg_u64 s[44:45], 0
	s_cselect_b64 s[4:5], s[4:5], s[38:39]
	s_lshr_b32 s38, s12, 3
	s_and_b32 s39, s12, 7
	s_lshl_b32 s8, s38, 17
	s_add_u32 s10, s10, s8
	s_lshl_b32 s8, s39, 7
	s_add_u32 s10, s10, s8
	s_add_u32 s4, s4, s10
	s_addc_u32 s5, s5, 0
	s_lshl_b32 s14, s14, 19
	s_lshr_b32 s8, s39, 2
	s_lshl_b32 s8, s8, 18
	s_add_u32 s14, s14, s8
	s_and_b32 s8, s39, 3
	s_lshl_b32 s8, s8, 15
	s_add_u32 s14, s14, s8
	s_lshl_b32 s8, s11, 17
	s_add_u32 s14, s14, s8
	s_lshl_b32 s8, s38, 7
	s_add_u32 s14, s14, s8
	s_add_u32 s92, s84, s14
	s_addc_u32 s93, s85, 0
	s_movk_i32 s25, 0x400
	s_movk_i32 s27, 0x1000
	s_movk_i32 s8, 0x400
	s_movk_i32 s9, 0x4000
	s_branch .Lcv1_goA1

; #define LAS __attribute__((address_space(3)))
; __device__ __forceinline__ void convert_experts(Frame& F, int lo, int hi) {
;     const int gw = F.vcu * 8 + F.wave, NGW = F.G * 8;
;     LAS unsigned char* scr = F.lds + F.wave * 16384;
;     unsigned char* W1t = WSP(F, WS_W1T, unsigned char); unsigned char* W2t = WSP(F, WS_W2T, unsigned char);
;     const float* weg = F.a->in[I_WEG]; const float* weu = F.a->in[I_WEU]; const float* wed = F.a->in[I_WED];
;     const float* wsg = F.a->in[I_WSG]; const float* wsu = F.a->in[I_WSU]; const float* wsd = F.a->in[I_WSD];
; __device__ __forceinline__ void router_topk(Frame& F, int tile) {
;     const float* logits = WSP(F, WS_B, float); const float* br = F.a->in[I_BR];
;     int* tk_e = WSP(F, WS_TOPK_E, int); float* tk_g = WSP(F, WS_TOPK_G, float); int* tk_p = WSP(F, WS_TOPK_P, int);
;     int* gcnt = (int*)(F.a->ws + WS_CTL + CTL_CNT);
;     LAS int* hist = (LAS int*)F.lds; LAS int* base = hist + 256;
;     const int lane = F.lane, w = F.wave;
;     if (F.tid < 256) hist[F.tid] = 0;
;     __syncthreads();
;     const f32x4 bias = *(const f32x4*)(br + 4 * lane);
;     f32x4 lgn = *(const f32x4*)(logits + (size_t)(tile * 256 + w * 32) * 256 + 4 * lane);
;     int pe = 0, pp = 0; float pg = 0.f;
;     int* dumpi = (int*)(F.a->ws + WS_B + ((size_t)128 << 20));
.LBB0_528:
	s_load_dword s64, s[0:1], 0xd0
	s_load_dwordx8 s[72:79], s[0:1], 0x80
	s_load_dwordx4 s[80:83], s[0:1], 0xa0
	s_load_dwordx2 s[84:85], s[0:1], 0xc0
	v_and_b32_e32 v46, 63, v0
	v_and_b32_e32 v47, 7, v46
	v_lshlrev_b32_e32 v47, 4, v47
	v_lshrrev_b32_e32 v46, 3, v46
	v_readfirstlane_b32 s40, v0
	s_waitcnt lgkmcnt(0)
	s_lshr_b32 s40, s40, 6
	s_and_b32 s39, s64, 7
	s_mov_b32 s41, s2
	s_cmp_lg_u32 s39, 0
	s_cbranch_scc1 .Lcvt_vcu
	s_and_b32 s39, s2, 7
	s_lshr_b32 s41, s64, 3
	s_mul_i32 s41, s41, s39
	s_lshr_b32 s39, s2, 3
	s_add_u32 s41, s41, s39
.Lcvt_vcu:
	s_and_b32 s69, s41, 7
	s_lshl_b32 s41, s41, 3
	s_add_u32 s89, s41, s40
	s_lshl_b32 s71, s64, 3
	s_mul_i32 s39, s71, 12
	s_add_u32 s89, s89, s39
	s_movk_i32 s90, 4
	s_mov_b32 s32, 0
	s_add_u32 s86, s84, 0x9180000
	s_addc_u32 s87, s85, 0
	s_add_u32 s84, s84, 0x1100000
	s_addc_u32 s85, s85, 0
	s_add_u32 s14, s8, 0x900000
	s_addc_u32 s15, s9, 0
	s_add_u32 s16, s8, 0xb00000
	s_addc_u32 s17, s9, 0
	s_add_u32 s18, s8, 0xd00000
	s_addc_u32 s19, s9, 0
	v_mov_b32_e32 v131, 0
	s_add_u32 s20, s8, 0x4000
	v_mov_b32_e32 v133, v131
	s_addc_u32 s21, s9, 0
	v_lshl_add_u64 v[2:3], s[8:9], 0, v[132:133]
	s_mov_b64 s[8:9], 0x1d1c0000
	s_waitcnt vmcnt(0)
	v_lshl_add_u64 v[12:13], v[2:3], 0, s[8:9]
	s_mov_b64 s[8:9], 0x1d1c0100
	s_movk_i32 s4, 0x100
	v_mov_b32_e32 v135, v131
	v_lshl_add_u64 v[14:15], v[2:3], 0, s[8:9]
	s_mov_b64 s[8:9], 0x1d1c0200
	v_cmp_gt_i32_e64 s[4:5], s4, v1
	s_mov_b32 s26, 0
	v_lshl_add_u32 v22, v1, 2, 0
	s_lshl_b32 s27, s49, 5
	v_lshl_add_u64 v[10:11], s[6:7], 0, v[134:135]
	v_cmp_gt_u32_e64 s[6:7], 8, v130
	v_lshl_add_u64 v[16:17], v[2:3], 0, s[8:9]
	v_mov_b64_e32 v[18:19], 0x100
	v_mov_b64_e32 v[20:21], 0xff
	v_mov_b32_e32 v23, 0xff800000
	v_mov_b32_e32 v24, 1
	s_waitcnt vmcnt(0)
	s_barrier
	s_branch .LBB0_532

; __device__ __forceinline__ void titem_finish(const TItem& t, int lane, const LAS unsigned char* buf) {
;     ...
;     if (t.f8) {
; #pragma unroll
;         for (int j = 0; j < 4; ++j) { const int n = (lane >> 3) + 8 * j;
;             int w0 = __builtin_amdgcn_cvt_pk_fp8_f32(v[j][0], v[j][1], 0, false); w0 = __builtin_amdgcn_cvt_pk_fp8_f32(v[j][2], v[j][3], w0, true);
;             int w1 = __builtin_amdgcn_cvt_pk_fp8_f32(v[j][4], v[j][5], 0, false); w1 = __builtin_amdgcn_cvt_pk_fp8_f32(v[j][6], v[j][7], w1, true);
;             u32x2 o; o.x = (unsigned)w0; o.y = (unsigned)w1;
;             __builtin_nontemporal_store(o, (u32x2*)((unsigned char*)t.WT + (size_t)(d0 + n) * t.K + k0 + 8 * c)); }
; __device__ __forceinline__ void router_topk(Frame& F, int tile) {
;     ...
;         const f32x4 lg = lgn;
;         {
;           const bool real = lane < 8 && i > 0; const size_t o = (size_t)(tok - 1) * 8 + lane;
;           int* de = real ? tk_e + o : dumpi + lane; float* dg = real ? tk_g + o : (float*)dumpi + 64 + lane; int* dp = real ? tk_p + o : dumpi + 128 + lane;
;           *de = pe; *dg = pg; *dp = pp; }
;         lgn = *(const f32x4*)(logits + (size_t)(i + 1 < 32 ? tok + 1 : tok) * 256 + 4 * lane);
.LBB0_543:
	s_or_b32 s8, s24, s22
	s_cmp_lg_u32 s24, 0
	s_cselect_b64 s[30:31], -1, 0
	s_ashr_i32 s9, s8, 31
	s_and_b64 vcc, s[6:7], s[30:31]
	s_lshl_b64 s[30:31], s[8:9], 3
	s_add_u32 s30, s30, -8
	s_addc_u32 s31, s31, -1
	s_cmp_eq_u32 s32, 1
	s_cbranch_scc1 .Lcvt_w16
	s_waitcnt vmcnt(0)
	s_cmp_eq_u32 s32, 2
	s_cbranch_scc0 .Lcvt_wd
	v_pk_mul_f32 v[48:49], v[48:49], s[94:95]
	v_pk_mul_f32 v[50:51], v[50:51], s[94:95]
	v_pk_mul_f32 v[52:53], v[52:53], s[94:95]
	v_pk_mul_f32 v[54:55], v[54:55], s[94:95]
	v_pk_mul_f32 v[56:57], v[56:57], s[94:95]
	v_pk_mul_f32 v[58:59], v[58:59], s[94:95]
	v_pk_mul_f32 v[60:61], v[60:61], s[94:95]
	v_pk_mul_f32 v[62:63], v[62:63], s[94:95]
	v_pk_mul_f32 v[64:65], v[64:65], s[94:95]
	v_pk_mul_f32 v[66:67], v[66:67], s[94:95]
	v_pk_mul_f32 v[68:69], v[68:69], s[94:95]
	v_pk_mul_f32 v[70:71], v[70:71], s[94:95]
	v_pk_mul_f32 v[72:73], v[72:73], s[94:95]
	v_pk_mul_f32 v[74:75], v[74:75], s[94:95]
	v_pk_mul_f32 v[76:77], v[76:77], s[94:95]
	v_pk_mul_f32 v[78:79], v[78:79], s[94:95]
	v_pk_mul_f32 v[80:81], v[80:81], s[94:95]
	v_pk_mul_f32 v[82:83], v[82:83], s[94:95]
	v_pk_mul_f32 v[84:85], v[84:85], s[94:95]
	v_pk_mul_f32 v[86:87], v[86:87], s[94:95]
	v_pk_mul_f32 v[88:89], v[88:89], s[94:95]
	v_pk_mul_f32 v[90:91], v[90:91], s[94:95]
	v_pk_mul_f32 v[92:93], v[92:93], s[94:95]
	v_pk_mul_f32 v[94:95], v[94:95], s[94:95]
	v_pk_mul_f32 v[96:97], v[96:97], s[94:95]
	v_pk_mul_f32 v[98:99], v[98:99], s[94:95]
	v_pk_mul_f32 v[100:101], v[100:101], s[94:95]
	v_pk_mul_f32 v[102:103], v[102:103], s[94:95]
	v_pk_mul_f32 v[104:105], v[104:105], s[94:95]
	v_pk_mul_f32 v[106:107], v[106:107], s[94:95]
	v_pk_mul_f32 v[108:109], v[108:109], s[94:95]
	v_pk_mul_f32 v[110:111], v[110:111], s[94:95]
	s_lshr_b32 s99, s36, 2
	v_lshlrev_b32_e32 v128, 4, v46
	v_cvt_pk_fp8_f32 v112, v48, v52
	v_cvt_pk_fp8_f32 v113, v64, v68
	v_cvt_pk_fp8_f32 v114, v80, v84
	v_cvt_pk_fp8_f32 v115, v96, v100
	v_cvt_pk_fp8_f32 v116, v49, v53
	v_cvt_pk_fp8_f32 v117, v65, v69
	v_cvt_pk_fp8_f32 v118, v81, v85
	v_cvt_pk_fp8_f32 v119, v97, v101
	v_cvt_pk_fp8_f32 v120, v50, v54
	v_cvt_pk_fp8_f32 v121, v66, v70
	v_cvt_pk_fp8_f32 v122, v82, v86
	v_cvt_pk_fp8_f32 v123, v98, v102
	v_cvt_pk_fp8_f32 v124, v51, v55
	v_cvt_pk_fp8_f32 v125, v67, v71
	v_cvt_pk_fp8_f32 v126, v83, v87
	v_cvt_pk_fp8_f32 v127, v99, v103
	v_mad_u32_u24 v128, v47, s99, v128
	v_add_u32_e32 v129, s36, v128
	s_lshl_b32 s99, s36, 1
	v_cvt_pk_fp8_f32 v112, v56, v60 op_sel:[0,0,1]
	v_cvt_pk_fp8_f32 v113, v72, v76 op_sel:[0,0,1]
	v_cvt_pk_fp8_f32 v114, v88, v92 op_sel:[0,0,1]
	v_cvt_pk_fp8_f32 v115, v104, v108 op_sel:[0,0,1]
	v_cvt_pk_fp8_f32 v116, v57, v61 op_sel:[0,0,1]
	v_cvt_pk_fp8_f32 v117, v73, v77 op_sel:[0,0,1]
	v_cvt_pk_fp8_f32 v118, v89, v93 op_sel:[0,0,1]
	v_cvt_pk_fp8_f32 v119, v105, v109 op_sel:[0,0,1]
	v_cvt_pk_fp8_f32 v120, v58, v62 op_sel:[0,0,1]
	v_cvt_pk_fp8_f32 v121, v74, v78 op_sel:[0,0,1]
	v_cvt_pk_fp8_f32 v122, v90, v94 op_sel:[0,0,1]
	v_cvt_pk_fp8_f32 v123, v106, v110 op_sel:[0,0,1]
	v_cvt_pk_fp8_f32 v124, v59, v63 op_sel:[0,0,1]
	v_cvt_pk_fp8_f32 v125, v75, v79 op_sel:[0,0,1]
	v_cvt_pk_fp8_f32 v126, v91, v95 op_sel:[0,0,1]
	v_cvt_pk_fp8_f32 v127, v107, v111 op_sel:[0,0,1]
	global_store_dwordx4 v128, v[112:115], s[92:93] nt
	global_store_dwordx4 v129, v[116:119], s[92:93] nt
	v_add_u32_e32 v128, s99, v128
	v_add_u32_e32 v129, s99, v129
	global_store_dwordx4 v128, v[120:123], s[92:93] nt
	global_store_dwordx4 v129, v[124:127], s[92:93] nt
	s_mov_b32 s32, 0
	s_branch .Lcvt_wd
.Lcvt_w16:
	s_waitcnt vmcnt(16)
	s_mov_b32 s32, 2
.Lcvt_wd:
	v_mov_b64_e32 v[30:31], v[8:9]
	s_cmp_lg_u32 s24, 31
	v_mov_b64_e32 v[28:29], v[6:7]
	v_lshl_add_u64 v[6:7], s[30:31], 0, v[130:131]
	s_cselect_b64 s[30:31], -1, 0
	v_lshlrev_b64 v[6:7], 2, v[6:7]
	s_cmp_lg_u64 s[30:31], 0
	v_lshl_add_u64 v[8:9], s[14:15], 0, v[6:7]
	v_lshl_add_u64 v[32:33], s[16:17], 0, v[6:7]
	v_lshl_add_u64 v[6:7], s[18:19], 0, v[6:7]
	s_addc_u32 s8, s8, 0
	v_cndmask_b32_e32 v9, v13, v9, vcc
	v_cndmask_b32_e32 v8, v12, v8, vcc
	v_cndmask_b32_e32 v6, v16, v6, vcc
	s_ashr_i32 s9, s8, 31
	v_cndmask_b32_e32 v33, v15, v33, vcc
	v_cndmask_b32_e32 v32, v14, v32, vcc
	v_cndmask_b32_e32 v7, v17, v7, vcc
	global_store_dword v[8:9], v27, off
	global_store_dword v[32:33], v26, off
	s_waitcnt lgkmcnt(0)
	global_store_dword v[6:7], v25, off
	v_mul_f32_e32 v6, 0xbfb8aa3b, v28
	s_lshl_b64 s[8:9], s[8:9], 10
	v_exp_f32_e32 v28, v6
	v_lshl_add_u64 v[6:7], v[10:11], 0, s[8:9]
	global_load_dwordx4 v[6:9], v[6:7], off
	s_sub_u32 s69, s69, 1
	s_cmp_lt_i32 s69, 0
	s_cbranch_scc0 .Lcvt_none_l
	s_mov_b32 s69, 7
	s_cmp_eq_u32 s90, 0
	s_cbranch_scc1 .Lcvt_none_l
	s_cmp_lg_u32 s32, 0
	s_cbranch_scc1 .Lcvt_none_l
	s_sub_u32 s90, s90, 1
	s_lshr_b32 s39, s89, 6
	s_and_b32 s40, s89, 63
	s_mul_hi_u32 s42, s39, 0xaaaaaaab
	s_lshr_b32 s42, s42, 1
	s_mul_i32 s41, s42, 3
	s_sub_u32 s41, s39, s41
	s_cmp_lt_u32 s42, 256
	s_cselect_b32 s100, s42, 0
	s_cselect_b64 s[44:45], -1, 0
	s_lshl_b32 s100, s100, 20
	s_cmp_eq_u32 s41, 2
	s_cbranch_scc1 .Lcvt_down_l
	s_cmp_eq_u32 s41, 0
	s_cselect_b64 s[96:97], s[72:73], s[74:75]
	s_cselect_b64 s[98:99], s[78:79], s[80:81]
	s_mov_b32 s94, 0xc3317218
	s_cselect_b32 s94, 0xc2b8aa3b, s94
	s_cmp_lg_u64 s[44:45], 0
	s_cselect_b64 s[96:97], s[96:97], s[98:99]
	s_lshr_b32 s55, s40, 3
	s_and_b32 s58, s40, 7
	s_lshl_b32 s39, s55, 17
	s_add_u32 s100, s100, s39
	s_lshl_b32 s39, s58, 7
	s_add_u32 s100, s100, s39
	s_add_u32 s96, s96, s100
	s_addc_u32 s97, s97, 0
	s_lshl_b32 s42, s42, 19
	s_lshr_b32 s39, s58, 2
	s_lshl_b32 s39, s39, 18
	s_add_u32 s42, s42, s39
	s_and_b32 s39, s58, 3
	s_lshl_b32 s39, s39, 15
	s_add_u32 s42, s42, s39
	s_lshl_b32 s39, s41, 17
	s_add_u32 s42, s42, s39
	s_lshl_b32 s39, s55, 7
	s_add_u32 s42, s42, s39
	s_add_u32 s92, s84, s42
	s_addc_u32 s93, s85, 0
	s_movk_i32 s36, 0x400
	s_movk_i32 s38, 0x1000
	s_movk_i32 s98, 0x400
	s_branch .Lcvt_go_l
; #define LAS __attribute__((address_space(3)))
; __device__ __forceinline__ void titem_issue(const TItem& t, int lane, LAS unsigned char* buf) {
;     const int nblk = t.N / 32, kb = t.item / nblk, nb = t.item % nblk, k0 = 64 * kb, n0 = 32 * nb;
; #pragma unroll
;     for (int j = 0; j < 8; ++j) { const float* g = t.W + (size_t)(k0 + 8 * j + (lane >> 3)) * t.N + n0 + 4 * ((lane & 7) ^ j);
;         __builtin_amdgcn_global_load_lds((const unsigned*)g, (LAS unsigned*)(buf + j * 1024), 16, 0, 2); }
; __device__ __forceinline__ void router_topk(Frame& F, int tile) {
;     ...
;         float sc[4], ch[4];
; #pragma unroll
;         for (int j = 0; j < 4; ++j) { sc[j] = fast_rcp(1.f + fast_exp2(-lg[j] * LOG2E)); ch[j] = sc[j] + bias[j]; }
;         float t1 = fmaxf(ch[0], ch[1]), t2 = fminf(ch[0], ch[1]);
;         { const float a = fmaxf(ch[2], ch[3]), b = fminf(ch[2], ch[3]); const float n1 = fmaxf(t1, a), n2 = fmaxf(fminf(t1, a), fmaxf(t2, b)); t1 = n1; t2 = n2; }
;         { const float a = dpp_f<0xB1>(t1, t1), b = dpp_f<0xB1>(t2, t2); const float n1 = fmaxf(t1, a), n2 = fmaxf(fminf(t1, a), fmaxf(t2, b)); t1 = n1; t2 = n2; }
;         { const float a = dpp_f<0x4E>(t1, t1), b = dpp_f<0x4E>(t2, t2); const float n1 = fmaxf(t1, a), n2 = fmaxf(fminf(t1, a), fmaxf(t2, b)); t1 = n1; t2 = n2; }
;         { const float a = dpp_f<0x141>(t1, t1), b = dpp_f<0x141>(t2, t2); const float n1 = fmaxf(t1, a), n2 = fmaxf(fminf(t1, a), fmaxf(t2, b)); t1 = n1; t2 = n2; }
;         const float gs = t1 + t2; int ngt = 0;
; #pragma unroll
;         for (int j = 0; j < 8; ++j) { const float o = __builtin_bit_cast(float, __builtin_amdgcn_readlane(__builtin_bit_cast(int, gs), 8 * j)); ngt += (o > gs) ? 1 : 0; }
;         const bool keep = ngt < 4;
; #pragma unroll
;         for (int j = 0; j < 4; ++j) ch[j] = keep ? ch[j] : -INFINITY;
;         unsigned a0, a1, a2, a3;
;         { unsigned kb_[4];
; #pragma unroll
;           for (int j = 0; j < 4; ++j) { const unsigned bts = __builtin_bit_cast(unsigned, ch[j]); kb_[j] = (bts & 0x80000000u) ? ~bts : (bts | 0x80000000u); }
;           a0 = kb_[0]; a1 = kb_[1]; a2 = kb_[2]; a3 = kb_[3]; }
;         float s0 = sc[0], s1 = sc[1], s2 = sc[2], s3 = sc[3]; int i0 = 0, i1 = 1, i2 = 2, i3 = 3;
;     ...
;         TK_CE(0, 1); TK_CE(2, 3); TK_CE(0, 2); TK_CE(1, 3); TK_CE(1, 2);
.Lcvt_down_l:
	s_cmp_lg_u64 s[44:45], 0
	s_cselect_b64 s[96:97], s[76:77], s[82:83]
	s_mov_b32 s94, 0x42800000
	s_lshr_b32 s55, s40, 5
	s_and_b32 s58, s40, 31
	s_lshl_b32 s39, s55, 19
	s_add_u32 s100, s100, s39
	s_lshl_b32 s39, s58, 7
	s_add_u32 s100, s100, s39
	s_add_u32 s96, s96, s100
	s_addc_u32 s97, s97, 0
	s_lshl_b32 s42, s42, 18
	s_lshl_b32 s39, s58, 13
	s_add_u32 s42, s42, s39
	s_lshl_b32 s39, s55, 7
	s_add_u32 s42, s42, s39
	s_add_u32 s92, s86, s42
	s_addc_u32 s93, s87, 0
	s_movk_i32 s36, 0x100
	s_movk_i32 s38, 0x400
	s_movk_i32 s98, 0x1000
.Lcvt_go_l:
	s_mov_b32 s95, s94
	s_lshl_b32 s99, s98, 4
	v_mad_u32_u24 v128, v46, s99, v47
	global_load_dwordx4 v[48:51], v128, s[96:97] nt
	s_add_u32 s96, s96, s98
	s_addc_u32 s97, s97, 0
	global_load_dwordx4 v[52:55], v128, s[96:97] nt
	s_add_u32 s96, s96, s98
	s_addc_u32 s97, s97, 0
	global_load_dwordx4 v[56:59], v128, s[96:97] nt
	s_add_u32 s96, s96, s98
	s_addc_u32 s97, s97, 0
	global_load_dwordx4 v[60:63], v128, s[96:97] nt
	s_add_u32 s96, s96, s98
	s_addc_u32 s97, s97, 0
	global_load_dwordx4 v[64:67], v128, s[96:97] nt
	s_add_u32 s96, s96, s98
	s_addc_u32 s97, s97, 0
	global_load_dwordx4 v[68:71], v128, s[96:97] nt
	s_add_u32 s96, s96, s98
	s_addc_u32 s97, s97, 0
	global_load_dwordx4 v[72:75], v128, s[96:97] nt
	s_add_u32 s96, s96, s98
	s_addc_u32 s97, s97, 0
	global_load_dwordx4 v[76:79], v128, s[96:97] nt
	s_add_u32 s96, s96, s98
	s_addc_u32 s97, s97, 0
	global_load_dwordx4 v[80:83], v128, s[96:97] nt
	s_add_u32 s96, s96, s98
	s_addc_u32 s97, s97, 0
	global_load_dwordx4 v[84:87], v128, s[96:97] nt
	s_add_u32 s96, s96, s98
	s_addc_u32 s97, s97, 0
	global_load_dwordx4 v[88:91], v128, s[96:97] nt
	s_add_u32 s96, s96, s98
	s_addc_u32 s97, s97, 0
	global_load_dwordx4 v[92:95], v128, s[96:97] nt
	s_add_u32 s96, s96, s98
	s_addc_u32 s97, s97, 0
	global_load_dwordx4 v[96:99], v128, s[96:97] nt
	s_add_u32 s96, s96, s98
	s_addc_u32 s97, s97, 0
	global_load_dwordx4 v[100:103], v128, s[96:97] nt
	s_add_u32 s96, s96, s98
	s_addc_u32 s97, s97, 0
	global_load_dwordx4 v[104:107], v128, s[96:97] nt
	s_add_u32 s96, s96, s98
	s_addc_u32 s97, s97, 0
	global_load_dwordx4 v[108:111], v128, s[96:97] nt
	s_add_u32 s89, s89, s71
	s_mov_b32 s32, 1
.Lcvt_none_l:
	v_mul_f32_e32 v30, 0xbfb8aa3b, v30
	v_mul_f32_e32 v29, 0xbfb8aa3b, v29
	v_exp_f32_e32 v30, v30
	v_mul_f32_e32 v31, 0xbfb8aa3b, v31
	v_exp_f32_e32 v31, v31
	v_exp_f32_e32 v29, v29
	v_add_f32_e32 v30, 1.0, v30
	v_add_f32_e32 v28, 1.0, v28
	v_rcp_f32_e32 v32, v30
	v_add_f32_e32 v30, 1.0, v31
	v_add_f32_e32 v29, 1.0, v29
	v_rcp_f32_e32 v28, v28
	v_rcp_f32_e32 v33, v30
	v_rcp_f32_e32 v29, v29
	v_add_f32_e32 v34, v4, v32
	s_mov_b32 s25, 0
	v_add_f32_e32 v35, v5, v33
	v_pk_add_f32 v[30:31], v[2:3], v[28:29]
	v_max_f32_e32 v36, v34, v35
	v_max_f32_e32 v38, v30, v31
	v_min_f32_e32 v37, v34, v35
	v_min_f32_e32 v39, v30, v31
	v_max_f32_e32 v40, v38, v36
	v_min_f32_e32 v36, v38, v36
	v_max3_f32 v36, v36, v39, v37
	v_mov_b32_e32 v37, v40
	v_mov_b32_e32 v38, v36
	s_nop 0
	v_mov_b32_dpp v37, v37 quad_perm:[1,0,3,2] row_mask:0xf bank_mask:0xf
	v_max_f32_e32 v37, v37, v37
	v_mov_b32_dpp v38, v38 quad_perm:[1,0,3,2] row_mask:0xf bank_mask:0xf
	v_max_f32_e32 v39, v40, v37
	v_min_f32_e32 v37, v40, v37
	v_max3_f32 v36, v37, v36, v38
	v_mov_b32_e32 v37, v39
	v_mov_b32_e32 v38, v36
	s_nop 0
	v_mov_b32_dpp v37, v37 quad_perm:[2,3,0,1] row_mask:0xf bank_mask:0xf
	v_max_f32_e32 v37, v37, v37
	v_mov_b32_dpp v38, v38 quad_perm:[2,3,0,1] row_mask:0xf bank_mask:0xf
	v_max_f32_e32 v40, v39, v37
	v_min_f32_e32 v37, v39, v37
	v_max3_f32 v36, v37, v36, v38
	v_mov_b32_e32 v37, v40
	v_mov_b32_e32 v38, v36
	s_nop 0
	v_mov_b32_dpp v37, v37 row_half_mirror row_mask:0xf bank_mask:0xf
	v_max_f32_e32 v37, v37, v37
	v_mov_b32_dpp v38, v38 row_half_mirror row_mask:0xf bank_mask:0xf
	v_max_f32_e32 v39, v40, v37
	v_min_f32_e32 v37, v40, v37
	v_max3_f32 v36, v37, v36, v38
	v_add_f32_e32 v36, v39, v36
	s_nop 0
	v_readlane_b32 s9, v36, 8
	v_readlane_b32 s8, v36, 0
	s_nop 0
	v_cmp_gt_f32_e32 vcc, s9, v36
	s_nop 1
	v_cndmask_b32_e64 v37, 0, 1, vcc
	v_cmp_gt_f32_e32 vcc, s8, v36
	v_readlane_b32 s8, v36, 16
	s_nop 0
	v_addc_co_u32_e32 v37, vcc, 0, v37, vcc
	v_cmp_gt_f32_e32 vcc, s8, v36
	v_readlane_b32 s8, v36, 24
	s_nop 0
	v_cndmask_b32_e64 v38, 0, 1, vcc
	v_cmp_gt_f32_e32 vcc, s8, v36
	v_readlane_b32 s8, v36, 32
	s_nop 0
	v_addc_co_u32_e32 v37, vcc, v37, v38, vcc
	v_cmp_gt_f32_e32 vcc, s8, v36
	v_readlane_b32 s8, v36, 40
	s_nop 0
	v_cndmask_b32_e64 v38, 0, 1, vcc
	v_cmp_gt_f32_e32 vcc, s8, v36
	v_readlane_b32 s8, v36, 48
	s_nop 0
	v_addc_co_u32_e32 v37, vcc, v37, v38, vcc
	v_cmp_gt_f32_e32 vcc, s8, v36
	v_readlane_b32 s8, v36, 56
	s_nop 0
	v_cndmask_b32_e64 v38, 0, 1, vcc
	v_cmp_gt_f32_e32 vcc, s8, v36
	s_nop 1
	v_addc_co_u32_e32 v36, vcc, v37, v38, vcc
	v_cmp_gt_u32_e32 vcc, 4, v36
	s_nop 1
	v_cndmask_b32_e32 v36, v23, v31, vcc
	v_cndmask_b32_e32 v37, v23, v30, vcc
	v_and_b32_e32 v31, 0x7fffffff, v36
	v_and_b32_e32 v30, 0x7fffffff, v37
	v_xor_b32_e32 v39, -1, v37
	v_pk_add_f32 v[30:31], v[30:31], 0 neg_lo:[1,1] neg_hi:[1,1]
	v_cmp_gt_i32_e64 s[8:9], 0, v37
	v_cndmask_b32_e32 v34, v23, v34, vcc
	v_xor_b32_e32 v38, -1, v36
	v_cndmask_b32_e64 v30, v30, v39, s[8:9]
	v_cmp_gt_i32_e64 s[8:9], 0, v36
	v_not_b32_e32 v36, v34
	v_or_b32_e32 v37, 0x80000000, v34
	v_cndmask_b32_e64 v31, v31, v38, s[8:9]
	v_cmp_gt_i32_e64 s[8:9], 0, v34
	v_cndmask_b32_e32 v35, v23, v35, vcc
	v_cmp_gt_i32_e32 vcc, 0, v35
	v_cndmask_b32_e64 v34, v37, v36, s[8:9]
	v_not_b32_e32 v36, v35
	v_cndmask_b32_e64 v35, -|v35|, v36, vcc
	v_cmp_gt_u32_e32 vcc, v31, v30
	v_max_u32_e32 v36, v31, v30
	v_min_u32_e32 v37, v31, v30
	v_cndmask_b32_e32 v38, v28, v29, vcc
	v_cndmask_b32_e32 v28, v29, v28, vcc
	v_cndmask_b32_e64 v29, 0, 1, vcc
	v_cmp_le_u32_e32 vcc, v31, v30
	v_max_u32_e32 v31, v35, v34
	v_min_u32_e32 v39, v35, v34
	v_cndmask_b32_e64 v30, 0, 1, vcc
	v_cmp_gt_u32_e32 vcc, v35, v34
	v_min_u32_e32 v42, v31, v36
	s_nop 0
	v_cndmask_b32_e32 v35, v32, v33, vcc
	v_cndmask_b32_e32 v32, v33, v32, vcc
	v_cndmask_b32_e64 v40, 2, 3, vcc
	v_cndmask_b32_e64 v41, 3, 2, vcc
	v_cmp_gt_u32_e32 vcc, v31, v36
	v_max_u32_e32 v33, v31, v36
	v_min_u32_e32 v36, v39, v37
	v_cndmask_b32_e32 v34, v38, v35, vcc
	v_cndmask_b32_e32 v31, v35, v38, vcc
	v_cndmask_b32_e32 v35, v29, v40, vcc
	v_cndmask_b32_e32 v43, v40, v29, vcc
	v_max_u32_e32 v40, v39, v37
	v_cmp_gt_u32_e32 vcc, v39, v37
	v_max_u32_e32 v37, v42, v40
	v_min_u32_e32 v38, v42, v40
	v_cndmask_b32_e32 v44, v28, v32, vcc
	v_cndmask_b32_e32 v28, v32, v28, vcc
	v_cndmask_b32_e32 v32, v30, v41, vcc
	v_cndmask_b32_e32 v29, v41, v30, vcc
	v_cmp_gt_u32_e32 vcc, v42, v40
	v_mov_b32_e32 v30, 0
	s_nop 0
	v_cndmask_b32_e32 v39, v44, v31, vcc
	v_cndmask_b32_e32 v40, v31, v44, vcc
	v_cndmask_b32_e32 v41, v32, v43, vcc
	v_cndmask_b32_e32 v42, v43, v32, vcc
	v_mov_b32_e32 v31, v130
	v_mov_b32_e32 v32, 0

; __device__ __forceinline__ void titem_finish(const TItem& t, int lane, const LAS unsigned char* buf) {
;     ...
;     if (t.f8) {
; #pragma unroll
;         for (int j = 0; j < 4; ++j) { const int n = (lane >> 3) + 8 * j;
;             int w0 = __builtin_amdgcn_cvt_pk_fp8_f32(v[j][0], v[j][1], 0, false); w0 = __builtin_amdgcn_cvt_pk_fp8_f32(v[j][2], v[j][3], w0, true);
;             int w1 = __builtin_amdgcn_cvt_pk_fp8_f32(v[j][4], v[j][5], 0, false); w1 = __builtin_amdgcn_cvt_pk_fp8_f32(v[j][6], v[j][7], w1, true);
;             u32x2 o; o.x = (unsigned)w0; o.y = (unsigned)w1;
;             __builtin_nontemporal_store(o, (u32x2*)((unsigned char*)t.WT + (size_t)(d0 + n) * t.K + k0 + 8 * c)); }
.LBB0_547:
	s_cmp_eq_u32 s32, 0
	s_cbranch_scc1 .Lcvt_al_done
	s_waitcnt vmcnt(0)
	v_pk_mul_f32 v[48:49], v[48:49], s[94:95]
	v_pk_mul_f32 v[50:51], v[50:51], s[94:95]
	v_pk_mul_f32 v[52:53], v[52:53], s[94:95]
	v_pk_mul_f32 v[54:55], v[54:55], s[94:95]
	v_pk_mul_f32 v[56:57], v[56:57], s[94:95]
	v_pk_mul_f32 v[58:59], v[58:59], s[94:95]
	v_pk_mul_f32 v[60:61], v[60:61], s[94:95]
	v_pk_mul_f32 v[62:63], v[62:63], s[94:95]
	v_pk_mul_f32 v[64:65], v[64:65], s[94:95]
	v_pk_mul_f32 v[66:67], v[66:67], s[94:95]
	v_pk_mul_f32 v[68:69], v[68:69], s[94:95]
	v_pk_mul_f32 v[70:71], v[70:71], s[94:95]
	v_pk_mul_f32 v[72:73], v[72:73], s[94:95]
	v_pk_mul_f32 v[74:75], v[74:75], s[94:95]
	v_pk_mul_f32 v[76:77], v[76:77], s[94:95]
	v_pk_mul_f32 v[78:79], v[78:79], s[94:95]
	v_pk_mul_f32 v[80:81], v[80:81], s[94:95]
	v_pk_mul_f32 v[82:83], v[82:83], s[94:95]
	v_pk_mul_f32 v[84:85], v[84:85], s[94:95]
	v_pk_mul_f32 v[86:87], v[86:87], s[94:95]
	v_pk_mul_f32 v[88:89], v[88:89], s[94:95]
	v_pk_mul_f32 v[90:91], v[90:91], s[94:95]
	v_pk_mul_f32 v[92:93], v[92:93], s[94:95]
	v_pk_mul_f32 v[94:95], v[94:95], s[94:95]
	v_pk_mul_f32 v[96:97], v[96:97], s[94:95]
	v_pk_mul_f32 v[98:99], v[98:99], s[94:95]
	v_pk_mul_f32 v[100:101], v[100:101], s[94:95]
	v_pk_mul_f32 v[102:103], v[102:103], s[94:95]
	v_pk_mul_f32 v[104:105], v[104:105], s[94:95]
	v_pk_mul_f32 v[106:107], v[106:107], s[94:95]
	v_pk_mul_f32 v[108:109], v[108:109], s[94:95]
	v_pk_mul_f32 v[110:111], v[110:111], s[94:95]
	s_lshr_b32 s99, s36, 2
	v_lshlrev_b32_e32 v128, 4, v46
	v_cvt_pk_fp8_f32 v112, v48, v52
	v_cvt_pk_fp8_f32 v113, v64, v68
	v_cvt_pk_fp8_f32 v114, v80, v84
	v_cvt_pk_fp8_f32 v115, v96, v100
	v_cvt_pk_fp8_f32 v116, v49, v53
	v_cvt_pk_fp8_f32 v117, v65, v69
	v_cvt_pk_fp8_f32 v118, v81, v85
	v_cvt_pk_fp8_f32 v119, v97, v101
	v_cvt_pk_fp8_f32 v120, v50, v54
	v_cvt_pk_fp8_f32 v121, v66, v70
	v_cvt_pk_fp8_f32 v122, v82, v86
	v_cvt_pk_fp8_f32 v123, v98, v102
	v_cvt_pk_fp8_f32 v124, v51, v55
	v_cvt_pk_fp8_f32 v125, v67, v71
	v_cvt_pk_fp8_f32 v126, v83, v87
	v_cvt_pk_fp8_f32 v127, v99, v103
	v_mad_u32_u24 v128, v47, s99, v128
	v_add_u32_e32 v129, s36, v128
	s_lshl_b32 s99, s36, 1
	v_cvt_pk_fp8_f32 v112, v56, v60 op_sel:[0,0,1]
	v_cvt_pk_fp8_f32 v113, v72, v76 op_sel:[0,0,1]
	v_cvt_pk_fp8_f32 v114, v88, v92 op_sel:[0,0,1]
	v_cvt_pk_fp8_f32 v115, v104, v108 op_sel:[0,0,1]
	v_cvt_pk_fp8_f32 v116, v57, v61 op_sel:[0,0,1]
	v_cvt_pk_fp8_f32 v117, v73, v77 op_sel:[0,0,1]
	v_cvt_pk_fp8_f32 v118, v89, v93 op_sel:[0,0,1]
	v_cvt_pk_fp8_f32 v119, v105, v109 op_sel:[0,0,1]
	v_cvt_pk_fp8_f32 v120, v58, v62 op_sel:[0,0,1]
	v_cvt_pk_fp8_f32 v121, v74, v78 op_sel:[0,0,1]
	v_cvt_pk_fp8_f32 v122, v90, v94 op_sel:[0,0,1]
	v_cvt_pk_fp8_f32 v123, v106, v110 op_sel:[0,0,1]
	v_cvt_pk_fp8_f32 v124, v59, v63 op_sel:[0,0,1]
	v_cvt_pk_fp8_f32 v125, v75, v79 op_sel:[0,0,1]
	v_cvt_pk_fp8_f32 v126, v91, v95 op_sel:[0,0,1]
	v_cvt_pk_fp8_f32 v127, v107, v111 op_sel:[0,0,1]
	global_store_dwordx4 v128, v[112:115], s[92:93] nt
	global_store_dwordx4 v129, v[116:119], s[92:93] nt
	v_add_u32_e32 v128, s99, v128
	v_add_u32_e32 v129, s99, v129
	global_store_dwordx4 v128, v[120:123], s[92:93] nt
	global_store_dwordx4 v129, v[124:127], s[92:93] nt
	s_mov_b32 s32, 0

; __device__ __forceinline__ void convert_experts(Frame& F, int lo, int hi) {
;     ...
;         for (;;) {
;             const bool more = sq + 1 < ns; const int rn = more ? CONV_RIDX(sq + 1) : r;
;             if (more) { CONV_DESC(rn, tn); titem_issue(tn, F.lane, scr + (p ^ 1) * 8192); }
;             if (!more) asm volatile("s_waitcnt vmcnt(0)" ::: "memory");
;             else if (first) asm volatile("s_waitcnt vmcnt(8)" ::: "memory");
;             else asm volatile("s_waitcnt vmcnt(12)" ::: "memory");
;             titem_finish(tc, F.lane, scr + p * 8192);
;             asm volatile("s_waitcnt lgkmcnt(0)" ::: "memory");
;             if (!more) break;
;             tc = tn; r = rn; ++sq; p ^= 1; first = false;
.LBB0_552:
.Lcvt_catch:
	s_cmp_eq_u32 s90, 0
	s_cbranch_scc1 .Lcvt_catch_done
	s_sub_u32 s90, s90, 1
	s_lshr_b32 s39, s89, 6
	s_and_b32 s40, s89, 63
	s_mul_hi_u32 s42, s39, 0xaaaaaaab
	s_lshr_b32 s42, s42, 1
	s_mul_i32 s41, s42, 3
	s_sub_u32 s41, s39, s41
	s_cmp_lt_u32 s42, 256
	s_cselect_b32 s100, s42, 0
	s_cselect_b64 s[44:45], -1, 0
	s_lshl_b32 s100, s100, 20
	s_cmp_eq_u32 s41, 2
	s_cbranch_scc1 .Lcvt_down_c
	s_cmp_eq_u32 s41, 0
	s_cselect_b64 s[96:97], s[72:73], s[74:75]
	s_cselect_b64 s[98:99], s[78:79], s[80:81]
	s_mov_b32 s94, 0xc3317218
	s_cselect_b32 s94, 0xc2b8aa3b, s94
	s_cmp_lg_u64 s[44:45], 0
	s_cselect_b64 s[96:97], s[96:97], s[98:99]
	s_lshr_b32 s55, s40, 3
	s_and_b32 s58, s40, 7
	s_lshl_b32 s39, s55, 17
	s_add_u32 s100, s100, s39
	s_lshl_b32 s39, s58, 7
	s_add_u32 s100, s100, s39
	s_add_u32 s96, s96, s100
	s_addc_u32 s97, s97, 0
	s_lshl_b32 s42, s42, 19
	s_lshr_b32 s39, s58, 2
	s_lshl_b32 s39, s39, 18
	s_add_u32 s42, s42, s39
	s_and_b32 s39, s58, 3
	s_lshl_b32 s39, s39, 15
	s_add_u32 s42, s42, s39
	s_lshl_b32 s39, s41, 17
	s_add_u32 s42, s42, s39
	s_lshl_b32 s39, s55, 7
	s_add_u32 s42, s42, s39
	s_add_u32 s92, s84, s42
	s_addc_u32 s93, s85, 0
	s_movk_i32 s36, 0x400
	s_movk_i32 s38, 0x1000
	s_movk_i32 s98, 0x400
	s_branch .Lcvt_go_c

; #define LAS __attribute__((address_space(3)))
; __device__ __forceinline__ void titem_issue(const TItem& t, int lane, LAS unsigned char* buf) {
;     const int nblk = t.N / 32, kb = t.item / nblk, nb = t.item % nblk, k0 = 64 * kb, n0 = 32 * nb;
; #pragma unroll
;     for (int j = 0; j < 8; ++j) { const float* g = t.W + (size_t)(k0 + 8 * j + (lane >> 3)) * t.N + n0 + 4 * ((lane & 7) ^ j);
;         __builtin_amdgcn_global_load_lds((const unsigned*)g, (LAS unsigned*)(buf + j * 1024), 16, 0, 2); }
; __device__ __forceinline__ void titem_finish(const TItem& t, int lane, const LAS unsigned char* buf) {
;     ...
;     if (t.f8) {
; #pragma unroll
;         for (int j = 0; j < 4; ++j) { const int n = (lane >> 3) + 8 * j;
;             int w0 = __builtin_amdgcn_cvt_pk_fp8_f32(v[j][0], v[j][1], 0, false); w0 = __builtin_amdgcn_cvt_pk_fp8_f32(v[j][2], v[j][3], w0, true);
;             int w1 = __builtin_amdgcn_cvt_pk_fp8_f32(v[j][4], v[j][5], 0, false); w1 = __builtin_amdgcn_cvt_pk_fp8_f32(v[j][6], v[j][7], w1, true);
;             u32x2 o; o.x = (unsigned)w0; o.y = (unsigned)w1;
;             __builtin_nontemporal_store(o, (u32x2*)((unsigned char*)t.WT + (size_t)(d0 + n) * t.K + k0 + 8 * c)); }
.Lcvt_go_c:
	s_mov_b32 s95, s94
	s_lshl_b32 s99, s98, 4
	v_mad_u32_u24 v128, v46, s99, v47
	global_load_dwordx4 v[48:51], v128, s[96:97] nt
	s_add_u32 s96, s96, s98
	s_addc_u32 s97, s97, 0
	global_load_dwordx4 v[52:55], v128, s[96:97] nt
	s_add_u32 s96, s96, s98
	s_addc_u32 s97, s97, 0
	global_load_dwordx4 v[56:59], v128, s[96:97] nt
	s_add_u32 s96, s96, s98
	s_addc_u32 s97, s97, 0
	global_load_dwordx4 v[60:63], v128, s[96:97] nt
	s_add_u32 s96, s96, s98
	s_addc_u32 s97, s97, 0
	global_load_dwordx4 v[64:67], v128, s[96:97] nt
	s_add_u32 s96, s96, s98
	s_addc_u32 s97, s97, 0
	global_load_dwordx4 v[68:71], v128, s[96:97] nt
	s_add_u32 s96, s96, s98
	s_addc_u32 s97, s97, 0
	global_load_dwordx4 v[72:75], v128, s[96:97] nt
	s_add_u32 s96, s96, s98
	s_addc_u32 s97, s97, 0
	global_load_dwordx4 v[76:79], v128, s[96:97] nt
	s_add_u32 s96, s96, s98
	s_addc_u32 s97, s97, 0
	global_load_dwordx4 v[80:83], v128, s[96:97] nt
	s_add_u32 s96, s96, s98
	s_addc_u32 s97, s97, 0
	global_load_dwordx4 v[84:87], v128, s[96:97] nt
	s_add_u32 s96, s96, s98
	s_addc_u32 s97, s97, 0
	global_load_dwordx4 v[88:91], v128, s[96:97] nt
	s_add_u32 s96, s96, s98
	s_addc_u32 s97, s97, 0
	global_load_dwordx4 v[92:95], v128, s[96:97] nt
	s_add_u32 s96, s96, s98
	s_addc_u32 s97, s97, 0
	global_load_dwordx4 v[96:99], v128, s[96:97] nt
	s_add_u32 s96, s96, s98
	s_addc_u32 s97, s97, 0
	global_load_dwordx4 v[100:103], v128, s[96:97] nt
	s_add_u32 s96, s96, s98
	s_addc_u32 s97, s97, 0
	global_load_dwordx4 v[104:107], v128, s[96:97] nt
	s_add_u32 s96, s96, s98
	s_addc_u32 s97, s97, 0
	global_load_dwordx4 v[108:111], v128, s[96:97] nt
	s_add_u32 s89, s89, s71
	s_waitcnt vmcnt(0)
	v_pk_mul_f32 v[48:49], v[48:49], s[94:95]
	v_pk_mul_f32 v[50:51], v[50:51], s[94:95]
	v_pk_mul_f32 v[52:53], v[52:53], s[94:95]
	v_pk_mul_f32 v[54:55], v[54:55], s[94:95]
	v_pk_mul_f32 v[56:57], v[56:57], s[94:95]
	v_pk_mul_f32 v[58:59], v[58:59], s[94:95]
	v_pk_mul_f32 v[60:61], v[60:61], s[94:95]
	v_pk_mul_f32 v[62:63], v[62:63], s[94:95]
	v_pk_mul_f32 v[64:65], v[64:65], s[94:95]
	v_pk_mul_f32 v[66:67], v[66:67], s[94:95]
	v_pk_mul_f32 v[68:69], v[68:69], s[94:95]
	v_pk_mul_f32 v[70:71], v[70:71], s[94:95]
	v_pk_mul_f32 v[72:73], v[72:73], s[94:95]
	v_pk_mul_f32 v[74:75], v[74:75], s[94:95]
	v_pk_mul_f32 v[76:77], v[76:77], s[94:95]
	v_pk_mul_f32 v[78:79], v[78:79], s[94:95]
	v_pk_mul_f32 v[80:81], v[80:81], s[94:95]
	v_pk_mul_f32 v[82:83], v[82:83], s[94:95]
	v_pk_mul_f32 v[84:85], v[84:85], s[94:95]
	v_pk_mul_f32 v[86:87], v[86:87], s[94:95]
	v_pk_mul_f32 v[88:89], v[88:89], s[94:95]
	v_pk_mul_f32 v[90:91], v[90:91], s[94:95]
	v_pk_mul_f32 v[92:93], v[92:93], s[94:95]
	v_pk_mul_f32 v[94:95], v[94:95], s[94:95]
	v_pk_mul_f32 v[96:97], v[96:97], s[94:95]
	v_pk_mul_f32 v[98:99], v[98:99], s[94:95]
	v_pk_mul_f32 v[100:101], v[100:101], s[94:95]
	v_pk_mul_f32 v[102:103], v[102:103], s[94:95]
	v_pk_mul_f32 v[104:105], v[104:105], s[94:95]
	v_pk_mul_f32 v[106:107], v[106:107], s[94:95]
	v_pk_mul_f32 v[108:109], v[108:109], s[94:95]
	v_pk_mul_f32 v[110:111], v[110:111], s[94:95]
	s_lshr_b32 s99, s36, 2
	v_lshlrev_b32_e32 v128, 4, v46
	v_cvt_pk_fp8_f32 v112, v48, v52
	v_cvt_pk_fp8_f32 v113, v64, v68
	v_cvt_pk_fp8_f32 v114, v80, v84
	v_cvt_pk_fp8_f32 v115, v96, v100
	v_cvt_pk_fp8_f32 v116, v49, v53
	v_cvt_pk_fp8_f32 v117, v65, v69
	v_cvt_pk_fp8_f32 v118, v81, v85
	v_cvt_pk_fp8_f32 v119, v97, v101
	v_cvt_pk_fp8_f32 v120, v50, v54
	v_cvt_pk_fp8_f32 v121, v66, v70
	v_cvt_pk_fp8_f32 v122, v82, v86
	v_cvt_pk_fp8_f32 v123, v98, v102
	v_cvt_pk_fp8_f32 v124, v51, v55
	v_cvt_pk_fp8_f32 v125, v67, v71
	v_cvt_pk_fp8_f32 v126, v83, v87
	v_cvt_pk_fp8_f32 v127, v99, v103
	v_mad_u32_u24 v128, v47, s99, v128
	v_add_u32_e32 v129, s36, v128
	s_lshl_b32 s99, s36, 1
	v_cvt_pk_fp8_f32 v112, v56, v60 op_sel:[0,0,1]
	v_cvt_pk_fp8_f32 v113, v72, v76 op_sel:[0,0,1]
	v_cvt_pk_fp8_f32 v114, v88, v92 op_sel:[0,0,1]
	v_cvt_pk_fp8_f32 v115, v104, v108 op_sel:[0,0,1]
	v_cvt_pk_fp8_f32 v116, v57, v61 op_sel:[0,0,1]
	v_cvt_pk_fp8_f32 v117, v73, v77 op_sel:[0,0,1]
	v_cvt_pk_fp8_f32 v118, v89, v93 op_sel:[0,0,1]
	v_cvt_pk_fp8_f32 v119, v105, v109 op_sel:[0,0,1]
	v_cvt_pk_fp8_f32 v120, v58, v62 op_sel:[0,0,1]
	v_cvt_pk_fp8_f32 v121, v74, v78 op_sel:[0,0,1]
	v_cvt_pk_fp8_f32 v122, v90, v94 op_sel:[0,0,1]
	v_cvt_pk_fp8_f32 v123, v106, v110 op_sel:[0,0,1]
	v_cvt_pk_fp8_f32 v124, v59, v63 op_sel:[0,0,1]
	v_cvt_pk_fp8_f32 v125, v75, v79 op_sel:[0,0,1]
	v_cvt_pk_fp8_f32 v126, v91, v95 op_sel:[0,0,1]
	v_cvt_pk_fp8_f32 v127, v107, v111 op_sel:[0,0,1]
	global_store_dwordx4 v128, v[112:115], s[92:93] nt
	global_store_dwordx4 v129, v[116:119], s[92:93] nt
	v_add_u32_e32 v128, s99, v128
	v_add_u32_e32 v129, s99, v129
	global_store_dwordx4 v128, v[120:123], s[92:93] nt
	global_store_dwordx4 v129, v[124:127], s[92:93] nt
	s_waitcnt vmcnt(0)
	s_branch .Lcvt_catch
